# speedup vs baseline: 1.0509x; 1.0509x over previous
.LBB2_22:
	s_cmp_eq_u32 s22, 0
	s_cselect_b64 s[4:5], -1, 0
	v_cmp_lt_i32_e64 s[40:41], s24, v91
	s_or_b32 s6, s24, 1
	v_cmp_lt_i32_e64 s[42:43], s6, v91
	s_or_b32 s6, s24, 2
	v_cmp_lt_i32_e64 s[44:45], s6, v91
	s_or_b32 s6, s24, 3
	v_cmp_lt_i32_e64 s[46:47], s6, v91
	s_mov_b64 s[20:21], exec
	s_and_b64 exec, s[20:21], s[40:41]
	s_cbranch_execz .Lgru_iss1
	v_cndmask_b32_e64 v230, v2, v6, s[4:5]
	v_mad_i64_i32 v[124:125], s[6:7], v230, s23, v[122:123]
	global_load_dwordx4 v[84:87], v[124:125], off
	global_load_dwordx4 v[80:83], v[124:125], off offset:64
	global_load_dwordx4 v[28:31], v[124:125], off offset:128
	global_load_dwordx4 v[24:27], v[124:125], off offset:192
	global_load_dwordx4 v[20:23], v[124:125], off offset:256
	global_load_dwordx4 v[10:13], v[124:125], off offset:320
	s_and_b64 exec, exec, vcc
	s_cbranch_execz .Lgru_iss1
	global_load_dwordx4 v[132:135], v[124:125], off offset:384
.Lgru_iss1:
	s_and_b64 exec, s[20:21], s[42:43]
	s_cbranch_execz .Lgru_iss2
	v_cndmask_b32_e64 v230, v3, v7, s[4:5]
	v_mad_i64_i32 v[224:225], s[6:7], v230, s23, v[122:123]
	global_load_dwordx4 v[136:139], v[224:225], off
	global_load_dwordx4 v[140:143], v[224:225], off offset:64
	global_load_dwordx4 v[144:147], v[224:225], off offset:128
	global_load_dwordx4 v[148:151], v[224:225], off offset:192
	global_load_dwordx4 v[152:155], v[224:225], off offset:256
	global_load_dwordx4 v[156:159], v[224:225], off offset:320
	s_and_b64 exec, exec, vcc
	s_cbranch_execz .Lgru_iss2
	global_load_dwordx4 v[160:163], v[224:225], off offset:384
.Lgru_iss2:
	s_and_b64 exec, s[20:21], s[44:45]
	s_cbranch_execz .Lgru_iss3
	v_cndmask_b32_e64 v230, v4, v8, s[4:5]
	v_mad_i64_i32 v[226:227], s[6:7], v230, s23, v[122:123]
	global_load_dwordx4 v[164:167], v[226:227], off
	global_load_dwordx4 v[168:171], v[226:227], off offset:64
	global_load_dwordx4 v[172:175], v[226:227], off offset:128
	global_load_dwordx4 v[180:183], v[226:227], off offset:192
	global_load_dwordx4 v[184:187], v[226:227], off offset:256
	global_load_dwordx4 v[188:191], v[226:227], off offset:320
	s_and_b64 exec, exec, vcc
	s_cbranch_execz .Lgru_iss3
	global_load_dwordx4 v[192:195], v[226:227], off offset:384
.Lgru_iss3:
	s_and_b64 exec, s[20:21], s[46:47]
	s_cbranch_execz .Lgru_iss4
	v_cndmask_b32_e64 v230, v5, v9, s[4:5]
	v_mad_i64_i32 v[228:229], s[6:7], v230, s23, v[122:123]
	global_load_dwordx4 v[196:199], v[228:229], off
	global_load_dwordx4 v[200:203], v[228:229], off offset:64
	global_load_dwordx4 v[204:207], v[228:229], off offset:128
	global_load_dwordx4 v[208:211], v[228:229], off offset:192
	global_load_dwordx4 v[212:215], v[228:229], off offset:256
	global_load_dwordx4 v[216:219], v[228:229], off offset:320
	s_and_b64 exec, exec, vcc
	s_cbranch_execz .Lgru_iss4
	global_load_dwordx4 v[220:223], v[228:229], off offset:384
.Lgru_iss4:
	s_waitcnt vmcnt(0)
	s_and_b64 exec, s[20:21], s[40:41]
	s_cbranch_execz .Lgru_acc1
	v_pk_add_f32 v[108:109], v[84:85], v[108:109]
	v_pk_add_f32 v[118:119], v[86:87], v[118:119]
	v_pk_add_f32 v[116:117], v[80:81], v[116:117]
	v_pk_add_f32 v[114:115], v[82:83], v[114:115]
	v_pk_add_f32 v[112:113], v[28:29], v[112:113]
	v_pk_add_f32 v[110:111], v[30:31], v[110:111]
	v_pk_add_f32 v[106:107], v[24:25], v[106:107]
	v_pk_add_f32 v[104:105], v[26:27], v[104:105]
	v_pk_add_f32 v[102:103], v[20:21], v[102:103]
	v_pk_add_f32 v[100:101], v[22:23], v[100:101]
	v_pk_add_f32 v[98:99], v[10:11], v[98:99]
	v_pk_add_f32 v[96:97], v[12:13], v[96:97]
	s_and_b64 exec, exec, vcc
	v_pk_add_f32 v[94:95], v[132:133], v[94:95]
	v_pk_add_f32 v[92:93], v[134:135], v[92:93]
.Lgru_acc1:
	s_and_b64 exec, s[20:21], s[42:43]
	s_cbranch_execz .Lgru_acc2
	v_pk_add_f32 v[108:109], v[136:137], v[108:109]
	v_pk_add_f32 v[118:119], v[138:139], v[118:119]
	v_pk_add_f32 v[116:117], v[140:141], v[116:117]
	v_pk_add_f32 v[114:115], v[142:143], v[114:115]
	v_pk_add_f32 v[112:113], v[144:145], v[112:113]
	v_pk_add_f32 v[110:111], v[146:147], v[110:111]
	v_pk_add_f32 v[106:107], v[148:149], v[106:107]
	v_pk_add_f32 v[104:105], v[150:151], v[104:105]
	v_pk_add_f32 v[102:103], v[152:153], v[102:103]
	v_pk_add_f32 v[100:101], v[154:155], v[100:101]
	v_pk_add_f32 v[98:99], v[156:157], v[98:99]
	v_pk_add_f32 v[96:97], v[158:159], v[96:97]
	s_and_b64 exec, exec, vcc
	v_pk_add_f32 v[94:95], v[160:161], v[94:95]
	v_pk_add_f32 v[92:93], v[162:163], v[92:93]
.Lgru_acc2:
	s_and_b64 exec, s[20:21], s[44:45]
	s_cbranch_execz .Lgru_acc3
	v_pk_add_f32 v[108:109], v[164:165], v[108:109]
	v_pk_add_f32 v[118:119], v[166:167], v[118:119]
	v_pk_add_f32 v[116:117], v[168:169], v[116:117]
	v_pk_add_f32 v[114:115], v[170:171], v[114:115]
	v_pk_add_f32 v[112:113], v[172:173], v[112:113]
	v_pk_add_f32 v[110:111], v[174:175], v[110:111]
	v_pk_add_f32 v[106:107], v[180:181], v[106:107]
	v_pk_add_f32 v[104:105], v[182:183], v[104:105]
	v_pk_add_f32 v[102:103], v[184:185], v[102:103]
	v_pk_add_f32 v[100:101], v[186:187], v[100:101]
	v_pk_add_f32 v[98:99], v[188:189], v[98:99]
	v_pk_add_f32 v[96:97], v[190:191], v[96:97]
	s_and_b64 exec, exec, vcc
	v_pk_add_f32 v[94:95], v[192:193], v[94:95]
	v_pk_add_f32 v[92:93], v[194:195], v[92:93]
.Lgru_acc3:
	s_and_b64 exec, s[20:21], s[46:47]
	s_cbranch_execz .Lgru_acc4
	v_pk_add_f32 v[108:109], v[196:197], v[108:109]
	v_pk_add_f32 v[118:119], v[198:199], v[118:119]
	v_pk_add_f32 v[116:117], v[200:201], v[116:117]
	v_pk_add_f32 v[114:115], v[202:203], v[114:115]
	v_pk_add_f32 v[112:113], v[204:205], v[112:113]
	v_pk_add_f32 v[110:111], v[206:207], v[110:111]
	v_pk_add_f32 v[106:107], v[208:209], v[106:107]
	v_pk_add_f32 v[104:105], v[210:211], v[104:105]
	v_pk_add_f32 v[102:103], v[212:213], v[102:103]
	v_pk_add_f32 v[100:101], v[214:215], v[100:101]
	v_pk_add_f32 v[98:99], v[216:217], v[98:99]
	v_pk_add_f32 v[96:97], v[218:219], v[96:97]
	s_and_b64 exec, exec, vcc
	v_pk_add_f32 v[94:95], v[220:221], v[94:95]
	v_pk_add_f32 v[92:93], v[222:223], v[92:93]
.Lgru_acc4:
	s_mov_b64 exec, s[20:21]
	s_add_i32 s24, s24, 4
	s_add_i32 s22, s22, -4
	v_cmp_ge_i32_e64 s[4:5], s24, v91
	s_or_b64 s[18:19], s[4:5], s[18:19]
	s_andn2_b64 exec, exec, s[18:19]
	s_cbranch_execnz .LBB2_22

	.amdhsa_kernel _Z10gru_kernelPKfPKiS2_S2_PK15HIP_vector_typeIiLj2EEPKDv8_DF16_S0_S0_Pfi
		.amdhsa_group_segment_fixed_size 30720
		.amdhsa_private_segment_fixed_size 0
		.amdhsa_kernarg_size 76
		.amdhsa_user_sgpr_count 2
		.amdhsa_user_sgpr_dispatch_ptr 0
		.amdhsa_user_sgpr_queue_ptr 0
		.amdhsa_user_sgpr_kernarg_segment_ptr 1
		.amdhsa_user_sgpr_dispatch_id 0
		.amdhsa_user_sgpr_kernarg_preload_length 0
		.amdhsa_user_sgpr_kernarg_preload_offset 0
		.amdhsa_user_sgpr_private_segment_size 0
		.amdhsa_uses_dynamic_stack 0
		.amdhsa_enable_private_segment 0
		.amdhsa_system_sgpr_workgroup_id_x 1
		.amdhsa_system_sgpr_workgroup_id_y 0
		.amdhsa_system_sgpr_workgroup_id_z 0
		.amdhsa_system_sgpr_workgroup_info 0
		.amdhsa_system_vgpr_workitem_id 0
		.amdhsa_next_free_vgpr 231
		.amdhsa_next_free_sgpr 96
		.amdhsa_accum_offset 232
		.amdhsa_reserve_vcc 1
		.amdhsa_float_round_mode_32 0
		.amdhsa_float_round_mode_16_64 0
		.amdhsa_float_denorm_mode_32 3
		.amdhsa_float_denorm_mode_16_64 3
		.amdhsa_dx10_clamp 1
		.amdhsa_ieee_mode 1
		.amdhsa_fp16_overflow 0
		.amdhsa_tg_split 0
		.amdhsa_exception_fp_ieee_invalid_op 0
		.amdhsa_exception_fp_denorm_src 0
		.amdhsa_exception_fp_ieee_div_zero 0
		.amdhsa_exception_fp_ieee_overflow 0
		.amdhsa_exception_fp_ieee_underflow 0
		.amdhsa_exception_fp_ieee_inexact 0
		.amdhsa_exception_int_div_zero 0
	.end_amdhsa_kernel

_Z9fc_kernelPKDv8_DF16_S1_Pf:
	s_cmp_gt_u32 s2, 255
	s_cbranch_scc1 .Lfc_exit
	s_load_dwordx4 s[4:7], s[0:1], 0x0
	s_load_dwordx2 s[16:17], s[0:1], 0x10
	v_and_b32_e32 v1, 63, v0
	v_lshrrev_b32_e32 v113, 6, v0
	v_and_b32_e32 v89, 31, v0
	v_bfe_u32 v90, v0, 5, 1
	v_lshlrev_b32_e32 v116, 4, v0
	v_lshlrev_b32_e32 v112, 4, v1
	v_lshlrev_b32_e32 v4, 12, v90
	v_lshl_or_b32 v4, v113, 8, v4
	v_lshl_or_b32 v4, v89, 2, v4
	v_add_u32_e32 v102, 0xe000, v4
	v_lshlrev_b32_e32 v5, 12, v113
	s_mov_b32 s3, 0xe000
	v_add3_u32 v103, v5, v112, s3
	v_mul_u32_u24_e32 v6, 0xc3500, v113
	v_add_u32_e32 v104, v6, v112
	v_add_u32_e32 v105, 0x30d40, v104
	v_add_u32_e32 v106, 0x61a80, v104
	v_add_u32_e32 v107, 0x927c0, v104
	v_add_u32_e32 v108, 0x30d400, v104
	v_add_u32_e32 v109, 0x30d400, v105
	v_add_u32_e32 v110, 0x30d400, v106
	v_add_u32_e32 v111, 0x30d400, v107
	v_mul_u32_u24_e32 v7, 0x3800, v113
	v_add_u32_e32 v114, v7, v112
	v_cmp_gt_u32_e64 s[34:35], 20, v1
	s_and_b32 s3, s2, 7
	s_lshl_b32 s3, s3, 5
	s_lshr_b32 s38, s2, 3
	s_add_i32 s38, s38, s3
	s_mov_b32 s20, 0
	s_mov_b32 s22, -1
	s_waitcnt lgkmcnt(0)
	s_lshl_b32 s29, s20, 8
	s_add_i32 s29, s29, s38
	s_cmp_lt_u32 s20, 12
	s_cbranch_scc1 .Lfc_t0
	s_lshr_b32 s29, s2, 2
	s_add_i32 s29, s29, 0xc00
.Lfc_t0:
	s_mul_hi_u32 s3, s29, 0x5397829d
	s_lshr_b32 s3, s3, 6
	s_mul_i32 s3, s3, 0xc4
	s_sub_i32 s3, s29, s3
	s_mul_i32 s3, s3, 0xe000
	v_add_u32_e32 v117, s3, v114
	v_add_u32_e32 v118, 0x1000, v117
	v_add_u32_e32 v119, 0x2000, v117
	v_add_u32_e32 v115, 0x3000, v117
	global_load_dwordx4 v[152:155], v117, s[4:5]
	global_load_dwordx4 v[156:159], v117, s[4:5] offset:1024
	global_load_dwordx4 v[160:163], v117, s[4:5] offset:2048
	global_load_dwordx4 v[164:167], v117, s[4:5] offset:3072
	global_load_dwordx4 v[168:171], v118, s[4:5]
	global_load_dwordx4 v[172:175], v118, s[4:5] offset:1024
	global_load_dwordx4 v[176:179], v118, s[4:5] offset:2048
	global_load_dwordx4 v[180:183], v118, s[4:5] offset:3072
	global_load_dwordx4 v[184:187], v119, s[4:5]
	global_load_dwordx4 v[188:191], v119, s[4:5] offset:1024
	global_load_dwordx4 v[192:195], v119, s[4:5] offset:2048
	global_load_dwordx4 v[196:199], v119, s[4:5] offset:3072
	global_load_dwordx4 v[200:203], v115, s[4:5]
	global_load_dwordx4 v[204:207], v115, s[4:5] offset:1024
.Lfc_seg:
	s_lshl_b32 s29, s20, 8
	s_add_i32 s29, s29, s38
	s_cmp_lt_u32 s20, 12
	s_cbranch_scc1 .Lfc_t1
	s_lshr_b32 s29, s2, 2
	s_add_i32 s29, s29, 0xc00
.Lfc_t1:
	s_mov_b32 s26, 0
	s_mov_b32 s23, 8
	s_cmp_lt_u32 s20, 12
	s_cbranch_scc1 .Lfc_full
	s_and_b32 s26, s2, 3
	s_lshl_b32 s26, s26, 1
	s_mov_b32 s23, 2
.Lfc_full:
	s_mul_hi_u32 s27, s29, 0x5397829d
	s_lshr_b32 s27, s27, 6
	s_mul_i32 s3, s27, 0xc4
	s_sub_i32 s28, s29, s3
	s_cmp_eq_u32 s20, 0
	s_cbranch_scc0 .Lfc_cw
	s_waitcnt vmcnt(0)
.Lfc_cw:
	s_waitcnt vmcnt(63)
	v_mov_b64_e32 v[32:33], v[152:153]
	v_mov_b64_e32 v[34:35], v[154:155]
	v_mov_b64_e32 v[36:37], v[156:157]
	v_mov_b64_e32 v[38:39], v[158:159]
	v_mov_b64_e32 v[40:41], v[160:161]
	v_mov_b64_e32 v[42:43], v[162:163]
	v_mov_b64_e32 v[44:45], v[164:165]
	v_mov_b64_e32 v[46:47], v[166:167]
	v_mov_b64_e32 v[48:49], v[168:169]
	v_mov_b64_e32 v[50:51], v[170:171]
	v_mov_b64_e32 v[52:53], v[172:173]
	v_mov_b64_e32 v[54:55], v[174:175]
	v_mov_b64_e32 v[56:57], v[176:177]
	v_mov_b64_e32 v[58:59], v[178:179]
	v_mov_b64_e32 v[60:61], v[180:181]
	v_mov_b64_e32 v[62:63], v[182:183]
	v_mov_b64_e32 v[64:65], v[184:185]
	v_mov_b64_e32 v[66:67], v[186:187]
	v_mov_b64_e32 v[68:69], v[188:189]
	v_mov_b64_e32 v[70:71], v[190:191]
	v_mov_b64_e32 v[72:73], v[192:193]
	v_mov_b64_e32 v[74:75], v[194:195]
	v_mov_b64_e32 v[76:77], v[196:197]
	v_mov_b64_e32 v[78:79], v[198:199]
	v_mov_b64_e32 v[80:81], v[200:201]
	v_mov_b64_e32 v[82:83], v[202:203]
	v_mov_b64_e32 v[84:85], v[204:205]
	v_mov_b64_e32 v[86:87], v[206:207]
	s_cmp_eq_u32 s27, s22
	s_cbranch_scc1 .Lfc_noA
	s_mov_b32 s22, s27
	s_mul_i32 s3, s27, 0xe000
	s_add_u32 s30, s6, s3
	s_addc_u32 s31, s7, 0
	global_load_dwordx4 v[152:155], v116, s[30:31]
	s_add_u32 s30, s30, 0x1000
	s_addc_u32 s31, s31, 0
	global_load_dwordx4 v[156:159], v116, s[30:31]
	s_add_u32 s30, s30, 0x1000
	s_addc_u32 s31, s31, 0
	global_load_dwordx4 v[160:163], v116, s[30:31]
	s_add_u32 s30, s30, 0x1000
	s_addc_u32 s31, s31, 0
	global_load_dwordx4 v[164:167], v116, s[30:31]
	s_add_u32 s30, s30, 0x1000
	s_addc_u32 s31, s31, 0
	global_load_dwordx4 v[168:171], v116, s[30:31]
	s_add_u32 s30, s30, 0x1000
	s_addc_u32 s31, s31, 0
	global_load_dwordx4 v[172:175], v116, s[30:31]
	s_add_u32 s30, s30, 0x1000
	s_addc_u32 s31, s31, 0
	global_load_dwordx4 v[176:179], v116, s[30:31]
	s_add_u32 s30, s30, 0x1000
	s_addc_u32 s31, s31, 0
	global_load_dwordx4 v[180:183], v116, s[30:31]
	s_add_u32 s30, s30, 0x1000
	s_addc_u32 s31, s31, 0
	global_load_dwordx4 v[184:187], v116, s[30:31]
	s_add_u32 s30, s30, 0x1000
	s_addc_u32 s31, s31, 0
	global_load_dwordx4 v[188:191], v116, s[30:31]
	s_add_u32 s30, s30, 0x1000
	s_addc_u32 s31, s31, 0
	global_load_dwordx4 v[192:195], v116, s[30:31]
	s_add_u32 s30, s30, 0x1000
	s_addc_u32 s31, s31, 0
	global_load_dwordx4 v[196:199], v116, s[30:31]
	s_add_u32 s30, s30, 0x1000
	s_addc_u32 s31, s31, 0
	global_load_dwordx4 v[200:203], v116, s[30:31]
	s_add_u32 s30, s30, 0x1000
	s_addc_u32 s31, s31, 0
	global_load_dwordx4 v[204:207], v116, s[30:31]
	s_barrier
	s_waitcnt vmcnt(0)
	ds_write_b128 v116, v[152:155]
	ds_write_b128 v116, v[156:159] offset:4096
	ds_write_b128 v116, v[160:163] offset:8192
	ds_write_b128 v116, v[164:167] offset:12288
	ds_write_b128 v116, v[168:171] offset:16384
	ds_write_b128 v116, v[172:175] offset:20480
	ds_write_b128 v116, v[176:179] offset:24576
	ds_write_b128 v116, v[180:183] offset:28672
	ds_write_b128 v116, v[184:187] offset:32768
	ds_write_b128 v116, v[188:191] offset:36864
	ds_write_b128 v116, v[192:195] offset:40960
	ds_write_b128 v116, v[196:199] offset:45056
	ds_write_b128 v116, v[200:203] offset:49152
	ds_write_b128 v116, v[204:207] offset:53248
	s_waitcnt lgkmcnt(0)
.Lfc_noA:
	s_add_i32 s36, s20, 1
	s_cmp_gt_u32 s36, 12
	s_cbranch_scc1 .Lfc_nopf
	s_lshl_b32 s37, s36, 8
	s_add_i32 s37, s37, s38
	s_cmp_lt_u32 s36, 12
	s_cbranch_scc1 .Lfc_t2
	s_lshr_b32 s37, s2, 2
	s_add_i32 s37, s37, 0xc00
.Lfc_t2:
	s_mul_hi_u32 s3, s37, 0x5397829d
	s_lshr_b32 s3, s3, 6
	s_mul_i32 s3, s3, 0xc4
	s_sub_i32 s3, s37, s3
	s_mul_i32 s3, s3, 0xe000
	v_add_u32_e32 v117, s3, v114
	v_add_u32_e32 v118, 0x1000, v117
	v_add_u32_e32 v119, 0x2000, v117
	v_add_u32_e32 v115, 0x3000, v117
	global_load_dwordx4 v[152:155], v117, s[4:5]
	global_load_dwordx4 v[156:159], v117, s[4:5] offset:1024
	global_load_dwordx4 v[160:163], v117, s[4:5] offset:2048
	global_load_dwordx4 v[164:167], v117, s[4:5] offset:3072
	global_load_dwordx4 v[168:171], v118, s[4:5]
	global_load_dwordx4 v[172:175], v118, s[4:5] offset:1024
	global_load_dwordx4 v[176:179], v118, s[4:5] offset:2048
	global_load_dwordx4 v[180:183], v118, s[4:5] offset:3072
	global_load_dwordx4 v[184:187], v119, s[4:5]
	global_load_dwordx4 v[188:191], v119, s[4:5] offset:1024
	global_load_dwordx4 v[192:195], v119, s[4:5] offset:2048
	global_load_dwordx4 v[196:199], v119, s[4:5] offset:3072
	global_load_dwordx4 v[200:203], v115, s[4:5]
	global_load_dwordx4 v[204:207], v115, s[4:5] offset:1024
.Lfc_nopf:
	s_lshl_b32 s3, s27, 8
	s_lshl_b32 s30, s26, 5
	s_add_i32 s3, s3, s30
	s_mul_i32 s3, s3, 0x30d40
	s_lshl_b32 s30, s28, 10
	s_add_u32 s3, s3, s30
	s_add_u32 s8, s16, s3
	s_addc_u32 s9, s17, 0
	s_mul_i32 s3, s26, 0x1c00
	v_add_u32_e32 v88, s3, v112
	s_mov_b64 s[24:25], -1
	s_cmp_eq_u32 s28, 195
	s_cselect_b64 s[24:25], s[34:35], s[24:25]
	s_mov_b32 s0, 0
	s_waitcnt lgkmcnt(0)
	s_barrier
.Lfc_step:
	ds_read_b128 v[120:123], v88
	ds_read_b128 v[124:127], v88 offset:1024
	ds_read_b128 v[128:131], v88 offset:2048
	ds_read_b128 v[132:135], v88 offset:3072
	ds_read_b128 v[136:139], v88 offset:4096
	ds_read_b128 v[140:143], v88 offset:5120
	ds_read_b128 v[144:147], v88 offset:6144
	v_add_u32_e32 v88, 0x1c00, v88
	s_waitcnt lgkmcnt(6)
	v_mfma_f32_32x32x16_f16 v[0:15], v[120:123], v[32:35], 0
	v_mfma_f32_32x32x16_f16 v[16:31], v[120:123], v[60:63], 0
	s_waitcnt lgkmcnt(5)
	v_mfma_f32_32x32x16_f16 v[0:15], v[124:127], v[36:39], v[0:15]
	v_mfma_f32_32x32x16_f16 v[16:31], v[124:127], v[64:67], v[16:31]
	s_waitcnt lgkmcnt(4)
	v_mfma_f32_32x32x16_f16 v[0:15], v[128:131], v[40:43], v[0:15]
	v_mfma_f32_32x32x16_f16 v[16:31], v[128:131], v[68:71], v[16:31]
	s_waitcnt lgkmcnt(3)
	v_mfma_f32_32x32x16_f16 v[0:15], v[132:135], v[44:47], v[0:15]
	v_mfma_f32_32x32x16_f16 v[16:31], v[132:135], v[72:75], v[16:31]
	s_waitcnt lgkmcnt(2)
	v_mfma_f32_32x32x16_f16 v[0:15], v[136:139], v[48:51], v[0:15]
	v_mfma_f32_32x32x16_f16 v[16:31], v[136:139], v[76:79], v[16:31]
	s_waitcnt lgkmcnt(1)
	v_mfma_f32_32x32x16_f16 v[0:15], v[140:143], v[52:55], v[0:15]
	v_mfma_f32_32x32x16_f16 v[16:31], v[140:143], v[80:83], v[16:31]
	s_waitcnt lgkmcnt(0)
	v_mfma_f32_32x32x16_f16 v[0:15], v[144:147], v[56:59], v[0:15]
	v_mfma_f32_32x32x16_f16 v[16:31], v[144:147], v[84:87], v[16:31]
	s_nop 11
	s_barrier
	ds_write_b32 v102, v0 offset:0
	ds_write_b32 v102, v1 offset:1024
	ds_write_b32 v102, v2 offset:2048
	ds_write_b32 v102, v3 offset:3072
	ds_write_b32 v102, v4 offset:8192
	ds_write_b32 v102, v5 offset:9216
	ds_write_b32 v102, v6 offset:10240
	ds_write_b32 v102, v7 offset:11264
	ds_write_b32 v102, v16 offset:128
	ds_write_b32 v102, v17 offset:1152
	ds_write_b32 v102, v18 offset:2176
	ds_write_b32 v102, v19 offset:3200
	ds_write_b32 v102, v20 offset:8320
	ds_write_b32 v102, v21 offset:9344
	ds_write_b32 v102, v22 offset:10368
	ds_write_b32 v102, v23 offset:11392
	s_waitcnt lgkmcnt(0)
	s_barrier
	ds_read_b128 v[0:3], v103
	ds_read_b128 v[4:7], v103 offset:1024
	ds_read_b128 v[16:19], v103 offset:2048
	ds_read_b128 v[20:23], v103 offset:3072
	s_mov_b64 exec, s[24:25]
	s_waitcnt lgkmcnt(3)
	global_store_dwordx4 v104, v[0:3], s[8:9]
	s_waitcnt lgkmcnt(2)
	global_store_dwordx4 v105, v[4:7], s[8:9]
	s_waitcnt lgkmcnt(1)
	global_store_dwordx4 v106, v[16:19], s[8:9]
	s_waitcnt lgkmcnt(0)
	global_store_dwordx4 v107, v[20:23], s[8:9]
	s_mov_b64 exec, -1
	s_barrier
	ds_write_b32 v102, v8 offset:0
	ds_write_b32 v102, v9 offset:1024
	ds_write_b32 v102, v10 offset:2048
	ds_write_b32 v102, v11 offset:3072
	ds_write_b32 v102, v12 offset:8192
	ds_write_b32 v102, v13 offset:9216
	ds_write_b32 v102, v14 offset:10240
	ds_write_b32 v102, v15 offset:11264
	ds_write_b32 v102, v24 offset:128
	ds_write_b32 v102, v25 offset:1152
	ds_write_b32 v102, v26 offset:2176
	ds_write_b32 v102, v27 offset:3200
	ds_write_b32 v102, v28 offset:8320
	ds_write_b32 v102, v29 offset:9344
	ds_write_b32 v102, v30 offset:10368
	ds_write_b32 v102, v31 offset:11392
	s_waitcnt lgkmcnt(0)
	s_barrier
	ds_read_b128 v[8:11], v103
	ds_read_b128 v[12:15], v103 offset:1024
	ds_read_b128 v[24:27], v103 offset:2048
	ds_read_b128 v[28:31], v103 offset:3072
	s_mov_b64 exec, s[24:25]
	s_waitcnt lgkmcnt(3)
	global_store_dwordx4 v108, v[8:11], s[8:9]
	s_waitcnt lgkmcnt(2)
	global_store_dwordx4 v109, v[12:15], s[8:9]
	s_waitcnt lgkmcnt(1)
	global_store_dwordx4 v110, v[24:27], s[8:9]
	s_waitcnt lgkmcnt(0)
	global_store_dwordx4 v111, v[28:31], s[8:9]
	s_mov_b64 exec, -1
	s_add_u32 s8, s8, 0x61a800
	s_addc_u32 s9, s9, 0
	s_add_i32 s0, s0, 1
	s_cmp_lt_u32 s0, s23
	s_cbranch_scc1 .Lfc_step
	s_add_i32 s20, s20, 1
	s_cmp_lt_u32 s20, 13
	s_cbranch_scc1 .Lfc_seg

	.amdhsa_kernel _Z9fc_kernelPKDv8_DF16_S1_Pf
		.amdhsa_group_segment_fixed_size 90112
		.amdhsa_private_segment_fixed_size 0
		.amdhsa_kernarg_size 24
		.amdhsa_user_sgpr_count 2
		.amdhsa_user_sgpr_dispatch_ptr 0
		.amdhsa_user_sgpr_queue_ptr 0
		.amdhsa_user_sgpr_kernarg_segment_ptr 1
		.amdhsa_user_sgpr_dispatch_id 0
		.amdhsa_user_sgpr_kernarg_preload_length 0
		.amdhsa_user_sgpr_kernarg_preload_offset 0
		.amdhsa_user_sgpr_private_segment_size 0
		.amdhsa_uses_dynamic_stack 0
		.amdhsa_enable_private_segment 0
		.amdhsa_system_sgpr_workgroup_id_x 1
		.amdhsa_system_sgpr_workgroup_id_y 0
		.amdhsa_system_sgpr_workgroup_id_z 0
		.amdhsa_system_sgpr_workgroup_info 0
		.amdhsa_system_vgpr_workitem_id 0
		.amdhsa_next_free_vgpr 208
		.amdhsa_next_free_sgpr 96
		.amdhsa_accum_offset 208
		.amdhsa_reserve_vcc 1
		.amdhsa_float_round_mode_32 0
		.amdhsa_float_round_mode_16_64 0
		.amdhsa_float_denorm_mode_32 3
		.amdhsa_float_denorm_mode_16_64 3
		.amdhsa_dx10_clamp 1
		.amdhsa_ieee_mode 1
		.amdhsa_fp16_overflow 0
		.amdhsa_tg_split 0
		.amdhsa_exception_fp_ieee_invalid_op 0
		.amdhsa_exception_fp_denorm_src 0
		.amdhsa_exception_fp_ieee_div_zero 0
		.amdhsa_exception_fp_ieee_overflow 0
		.amdhsa_exception_fp_ieee_underflow 0
		.amdhsa_exception_fp_ieee_inexact 0
		.amdhsa_exception_int_div_zero 0
	.end_amdhsa_kernel

amdhsa.kernels:
  - .agpr_count:     0
    .args:
      - .actual_access:  read_only
        .address_space:  global
        .offset:         0
        .size:           8
        .value_kind:     global_buffer
      - .actual_access:  read_only
        .address_space:  global
        .offset:         8
        .size:           8
        .value_kind:     global_buffer
      - .actual_access:  read_only
        .address_space:  global
        .offset:         16
        .size:           8
        .value_kind:     global_buffer
      - .actual_access:  read_only
        .address_space:  global
        .offset:         24
        .size:           8
        .value_kind:     global_buffer
      - .actual_access:  read_only
        .address_space:  global
        .offset:         32
        .size:           8
        .value_kind:     global_buffer
      - .actual_access:  write_only
        .address_space:  global
        .offset:         40
        .size:           8
        .value_kind:     global_buffer
      - .actual_access:  write_only
        .address_space:  global
        .offset:         48
        .size:           8
        .value_kind:     global_buffer
      - .actual_access:  write_only
        .address_space:  global
        .offset:         56
        .size:           8
        .value_kind:     global_buffer
    .group_segment_fixed_size: 0
    .kernarg_segment_align: 8
    .kernarg_segment_size: 64
    .language:       OpenCL C
    .language_version:
      - 2
      - 0
    .max_flat_workgroup_size: 256
    .name:           _Z11prep_kernelPKfS0_S0_S0_S0_PDv8_DF16_S2_Pi
    .private_segment_fixed_size: 0
    .sgpr_count:     26
    .sgpr_spill_count: 0
    .symbol:         _Z11prep_kernelPKfS0_S0_S0_S0_PDv8_DF16_S2_Pi.kd
    .uniform_work_group_size: 1
    .uses_dynamic_stack: false
    .vgpr_count:     18
    .vgpr_spill_count: 0
    .wavefront_size: 64
  - .agpr_count:     0
    .args:
      - .actual_access:  read_only
        .address_space:  global
        .offset:         0
        .size:           8
        .value_kind:     global_buffer
      - .actual_access:  read_only
        .address_space:  global
        .offset:         8
        .size:           8
        .value_kind:     global_buffer
      - .actual_access:  read_only
        .address_space:  global
        .offset:         16
        .size:           8
        .value_kind:     global_buffer
      - .actual_access:  read_only
        .address_space:  global
        .offset:         24
        .size:           8
        .value_kind:     global_buffer
      - .actual_access:  read_only
        .address_space:  global
        .offset:         32
        .size:           8
        .value_kind:     global_buffer
      - .actual_access:  read_only
        .address_space:  global
        .offset:         40
        .size:           8
        .value_kind:     global_buffer
      - .actual_access:  read_only
        .address_space:  global
        .offset:         48
        .size:           8
        .value_kind:     global_buffer
      - .actual_access:  read_only
        .address_space:  global
        .offset:         56
        .size:           8
        .value_kind:     global_buffer
      - .actual_access:  read_only
        .address_space:  global
        .offset:         64
        .size:           8
        .value_kind:     global_buffer
      - .actual_access:  read_only
        .address_space:  global
        .offset:         72
        .size:           8
        .value_kind:     global_buffer
      - .actual_access:  read_only
        .address_space:  global
        .offset:         80
        .size:           8
        .value_kind:     global_buffer
      - .actual_access:  read_only
        .address_space:  global
        .offset:         88
        .size:           8
        .value_kind:     global_buffer
      - .actual_access:  read_only
        .address_space:  global
        .offset:         96
        .size:           8
        .value_kind:     global_buffer
      - .actual_access:  read_only
        .address_space:  global
        .offset:         104
        .size:           8
        .value_kind:     global_buffer
      - .actual_access:  write_only
        .address_space:  global
        .offset:         112
        .size:           8
        .value_kind:     global_buffer
      - .offset:         120
        .size:           4
        .value_kind:     by_value
      - .actual_access:  read_only
        .address_space:  global
        .offset:         128
        .size:           8
        .value_kind:     global_buffer
      - .actual_access:  read_only
        .address_space:  global
        .offset:         136
        .size:           8
        .value_kind:     global_buffer
      - .actual_access:  write_only
        .address_space:  global
        .offset:         144
        .size:           8
        .value_kind:     global_buffer
      - .actual_access:  read_only
        .address_space:  global
        .offset:         152
        .size:           8
        .value_kind:     global_buffer
      - .actual_access:  read_only
        .address_space:  global
        .offset:         160
        .size:           8
        .value_kind:     global_buffer
      - .address_space:  global
        .offset:         168
        .size:           8
        .value_kind:     global_buffer
      - .actual_access:  write_only
        .address_space:  global
        .offset:         176
        .size:           8
        .value_kind:     global_buffer
      - .address_space:  global
        .offset:         184
        .size:           8
        .value_kind:     global_buffer
      - .actual_access:  write_only
        .address_space:  global
        .offset:         192
        .size:           8
        .value_kind:     global_buffer
      - .actual_access:  write_only
        .address_space:  global
        .offset:         200
        .size:           8
        .value_kind:     global_buffer
    .group_segment_fixed_size: 21760
    .kernarg_segment_align: 8
    .kernarg_segment_size: 208
    .language:       OpenCL C
    .language_version:
      - 2
      - 0
    .max_flat_workgroup_size: 256
    .name:           _Z12embed_kernelPKiS0_S0_S0_S0_PKfS2_S2_S2_S2_S2_S2_S2_PKDv8_DF16_PfiS2_S2_PS3_S0_S0_PiS8_S8_P15HIP_vector_typeIiLj2EES8_
    .private_segment_fixed_size: 0
    .sgpr_count:     44
    .sgpr_spill_count: 0
    .symbol:         _Z12embed_kernelPKiS0_S0_S0_S0_PKfS2_S2_S2_S2_S2_S2_S2_PKDv8_DF16_PfiS2_S2_PS3_S0_S0_PiS8_S8_P15HIP_vector_typeIiLj2EES8_.kd
    .uniform_work_group_size: 1
    .uses_dynamic_stack: false
    .vgpr_count:     166
    .vgpr_spill_count: 0
    .wavefront_size: 64
  - .agpr_count:     0
    .args:
      - .actual_access:  read_only
        .address_space:  global
        .offset:         0
        .size:           8
        .value_kind:     global_buffer
      - .actual_access:  read_only
        .address_space:  global
        .offset:         8
        .size:           8
        .value_kind:     global_buffer
      - .actual_access:  read_only
        .address_space:  global
        .offset:         16
        .size:           8
        .value_kind:     global_buffer
      - .actual_access:  read_only
        .address_space:  global
        .offset:         24
        .size:           8
        .value_kind:     global_buffer
      - .actual_access:  read_only
        .address_space:  global
        .offset:         32
        .size:           8
        .value_kind:     global_buffer
      - .actual_access:  read_only
        .address_space:  global
        .offset:         40
        .size:           8
        .value_kind:     global_buffer
      - .actual_access:  read_only
        .address_space:  global
        .offset:         48
        .size:           8
        .value_kind:     global_buffer
      - .actual_access:  read_only
        .address_space:  global
        .offset:         56
        .size:           8
        .value_kind:     global_buffer
      - .actual_access:  write_only
        .address_space:  global
        .offset:         64
        .size:           8
        .value_kind:     global_buffer
      - .offset:         72
        .size:           4
        .value_kind:     by_value
    .group_segment_fixed_size: 30720
    .kernarg_segment_align: 8
    .kernarg_segment_size: 76
    .language:       OpenCL C
    .language_version:
      - 2
      - 0
    .max_flat_workgroup_size: 256
    .name:           _Z10gru_kernelPKfPKiS2_S2_PK15HIP_vector_typeIiLj2EEPKDv8_DF16_S0_S0_Pfi
    .private_segment_fixed_size: 0
    .sgpr_count:     31
    .sgpr_spill_count: 0
    .symbol:         _Z10gru_kernelPKfPKiS2_S2_PK15HIP_vector_typeIiLj2EEPKDv8_DF16_S0_S0_Pfi.kd
    .uniform_work_group_size: 1
    .uses_dynamic_stack: false
    .vgpr_count:     231
    .vgpr_spill_count: 0
    .wavefront_size: 64
  - .agpr_count:     0
    .args:
      - .actual_access:  read_only
        .address_space:  global
        .offset:         0
        .size:           8
        .value_kind:     global_buffer
      - .actual_access:  read_only
        .address_space:  global
        .offset:         8
        .size:           8
        .value_kind:     global_buffer
      - .actual_access:  write_only
        .address_space:  global
        .offset:         16
        .size:           8
        .value_kind:     global_buffer
    .group_segment_fixed_size: 1024
    .kernarg_segment_align: 8
    .kernarg_segment_size: 24
    .language:       OpenCL C
    .language_version:
      - 2
      - 0
    .max_flat_workgroup_size: 256
    .name:           _Z11pool_kernelPKfPKiPDF16_
    .private_segment_fixed_size: 0
    .sgpr_count:     16
    .sgpr_spill_count: 0
    .symbol:         _Z11pool_kernelPKfPKiPDF16_.kd
    .uniform_work_group_size: 1
    .uses_dynamic_stack: false
    .vgpr_count:     18
    .vgpr_spill_count: 0
    .wavefront_size: 64
  - .agpr_count:     0
    .args:
      - .actual_access:  read_only
        .address_space:  global
        .offset:         0
        .size:           8
        .value_kind:     global_buffer
      - .actual_access:  read_only
        .address_space:  global
        .offset:         8
        .size:           8
        .value_kind:     global_buffer
      - .actual_access:  write_only
        .address_space:  global
        .offset:         16
        .size:           8
        .value_kind:     global_buffer
    .group_segment_fixed_size: 90112
    .kernarg_segment_align: 8
    .kernarg_segment_size: 24
    .language:       OpenCL C
    .language_version:
      - 2
      - 0
    .max_flat_workgroup_size: 256
    .name:           _Z9fc_kernelPKDv8_DF16_S1_Pf
    .private_segment_fixed_size: 0
    .sgpr_count:     17
    .sgpr_spill_count: 0
    .symbol:         _Z9fc_kernelPKDv8_DF16_S1_Pf.kd
    .uniform_work_group_size: 1
    .uses_dynamic_stack: false
    .vgpr_count:     208
    .vgpr_spill_count: 0
    .wavefront_size: 64
